# final_kernel: gather index guard as one v_min inside the masked blocks (one VALU and one s_nop fewer per record)
# speedup vs baseline: 1.0097x; 1.0015x over previous
.LBB2_4:
	s_or_b64 exec, exec, s[4:5]
	s_load_dwordx2 s[26:27], s[0:1], 0x0
	v_lshlrev_b32_e32 v36, 3, v0
	s_and_saveexec_b64 s[4:5], s[2:3]
	v_mov_b32_e32 v4, 0
	v_mov_b32_e32 v5, v4
	ds_write_b64 v36, v[4:5]
	s_or_b64 exec, exec, s[4:5]
	s_load_dwordx2 s[24:25], s[0:1], 0x10
	v_cmp_eq_u32_e64 s[2:3], 0, v0
	s_and_saveexec_b64 s[4:5], s[2:3]
	v_mov_b32_e32 v4, 0
	ds_write_b32 v4, v4 offset:1568
	s_or_b64 exec, exec, s[4:5]
	v_mul_u32_u24_e32 v26, 0x1f40, v1
	v_mov_b32_e32 v27, 0
	v_max_i32_e32 v1, 1, v35
	v_and_b32_e32 v37, 3, v0
	v_lshl_add_u64 v[2:3], v[2:3], 0, v[26:27]
	v_add_u32_e32 v6, -1, v1
	v_lshlrev_b32_e32 v1, 1, v37
	v_cndmask_b32_e32 v23, 0, v3, vcc
	v_cndmask_b32_e32 v22, 0, v2, vcc
	v_min_u32_e32 v2, v1, v6
	v_or_b32_e32 v30, 8, v1
	s_waitcnt lgkmcnt(0)
	v_lshl_add_u64 v[28:29], v[22:23], 3, s[26:27]
	v_lshlrev_b32_e32 v26, 3, v2
	v_min_u32_e32 v4, v30, v6
	v_lshl_add_u64 v[2:3], v[28:29], 0, v[26:27]
	v_lshlrev_b32_e32 v26, 3, v4
	v_or_b32_e32 v25, 16, v1
	v_lshl_add_u64 v[4:5], v[28:29], 0, v[26:27]
	global_load_dwordx4 v[14:17], v[2:3], off
	global_load_dwordx4 v[10:13], v[4:5], off
	v_min_u32_e32 v2, v25, v6
	v_or_b32_e32 v24, 24, v1
	v_lshlrev_b32_e32 v26, 3, v2
	v_min_u32_e32 v2, v24, v6
	v_lshl_add_u64 v[32:33], v[28:29], 0, v[26:27]
	v_lshlrev_b32_e32 v26, 3, v2
	v_lshl_add_u64 v[38:39], v[28:29], 0, v[26:27]
	global_load_dwordx4 v[6:9], v[32:33], off
	global_load_dwordx4 v[2:5], v[38:39], off
	v_cmp_lt_i32_e64 s[16:17], v1, v35
	v_mov_b32_e32 v26, 0
	s_and_saveexec_b64 s[2:3], s[16:17]
	s_cbranch_execz .LBB2_10
	s_waitcnt vmcnt(3)
	v_and_b32_e32 v26, 0x7ffff, v14
	v_min_u32_e32 v26, 0x7a11f, v26
	v_lshlrev_b32_e32 v26, 2, v26
	global_load_dword v26, v26, s[24:25]
	s_waitcnt vmcnt(0)
	v_mul_f32_e32 v26, v15, v26
.LBB2_10:
	s_or_b64 exec, exec, s[2:3]
	s_waitcnt vmcnt(3)
	v_or_b32_e32 v15, 1, v1
	v_cmp_lt_i32_e64 s[14:15], v15, v35
	s_and_saveexec_b64 s[2:3], s[14:15]
	s_cbranch_execz .LBB2_12
	v_and_b32_e32 v15, 0x7ffff, v16
	v_min_u32_e32 v15, 0x7a11f, v15
	v_lshlrev_b32_e32 v15, 2, v15
	global_load_dword v15, v15, s[24:25]
	s_waitcnt vmcnt(0)
	v_mul_f32_e32 v27, v17, v15
.LBB2_12:
	s_or_b64 exec, exec, s[2:3]
	v_cmp_lt_i32_e64 s[12:13], v30, v35
	v_mov_b32_e32 v15, 0
	v_mov_b32_e32 v17, 0
	s_and_saveexec_b64 s[2:3], s[12:13]
	s_cbranch_execz .LBB2_14
	s_waitcnt vmcnt(2)
	v_and_b32_e32 v17, 0x7ffff, v10
	v_min_u32_e32 v17, 0x7a11f, v17
	v_lshlrev_b32_e32 v17, 2, v17
	global_load_dword v17, v17, s[24:25]
	s_waitcnt vmcnt(0)
	v_mul_f32_e32 v17, v11, v17
.LBB2_14:
	s_or_b64 exec, exec, s[2:3]
	s_waitcnt vmcnt(2)
	v_or_b32_e32 v11, 9, v1
	v_cmp_lt_i32_e64 s[10:11], v11, v35
	s_and_saveexec_b64 s[2:3], s[10:11]
	s_cbranch_execz .LBB2_16
	v_and_b32_e32 v11, 0x7ffff, v12
	v_min_u32_e32 v11, 0x7a11f, v11
	v_lshlrev_b32_e32 v11, 2, v11
	global_load_dword v11, v11, s[24:25]
	s_waitcnt vmcnt(0)
	v_mul_f32_e32 v15, v13, v11
.LBB2_16:
	s_or_b64 exec, exec, s[2:3]
	v_cmp_lt_i32_e64 s[8:9], v25, v35
	v_mov_b32_e32 v11, 0
	v_mov_b32_e32 v13, 0
	s_and_saveexec_b64 s[2:3], s[8:9]
	s_cbranch_execz .LBB2_18
	s_waitcnt vmcnt(1)
	v_and_b32_e32 v13, 0x7ffff, v6
	v_min_u32_e32 v13, 0x7a11f, v13
	v_lshlrev_b32_e32 v13, 2, v13
	global_load_dword v13, v13, s[24:25]
	s_waitcnt vmcnt(0)
	v_mul_f32_e32 v13, v7, v13
.LBB2_18:
	s_or_b64 exec, exec, s[2:3]
	s_waitcnt vmcnt(1)
	v_or_b32_e32 v7, 17, v1
	v_cmp_lt_i32_e64 s[6:7], v7, v35
	s_and_saveexec_b64 s[2:3], s[6:7]
	s_cbranch_execz .LBB2_20
	v_and_b32_e32 v7, 0x7ffff, v8
	v_min_u32_e32 v7, 0x7a11f, v7
	v_lshlrev_b32_e32 v7, 2, v7
	global_load_dword v7, v7, s[24:25]
	s_waitcnt vmcnt(0)
	v_mul_f32_e32 v11, v9, v7
.LBB2_20:
	s_or_b64 exec, exec, s[2:3]
	v_cmp_lt_i32_e64 s[4:5], v24, v35
	v_mov_b32_e32 v7, 0
	v_mov_b32_e32 v9, 0
	s_and_saveexec_b64 s[2:3], s[4:5]
	s_cbranch_execz .LBB2_22
	s_waitcnt vmcnt(0)
	v_and_b32_e32 v9, 0x7ffff, v2
	v_min_u32_e32 v9, 0x7a11f, v9
	v_lshlrev_b32_e32 v9, 2, v9
	global_load_dword v9, v9, s[24:25]
	s_waitcnt vmcnt(0)
	v_mul_f32_e32 v9, v3, v9
.LBB2_22:
	s_or_b64 exec, exec, s[2:3]
	v_or_b32_e32 v1, 25, v1
	v_cmp_lt_i32_e32 vcc, v1, v35
	s_and_saveexec_b64 s[18:19], vcc
	s_cbranch_execz .LBB2_24
	s_waitcnt vmcnt(0)
	v_and_b32_e32 v1, 0x7ffff, v4
	v_min_u32_e32 v1, 0x7a11f, v1
	v_lshlrev_b32_e32 v1, 2, v1
	global_load_dword v1, v1, s[24:25]
	s_waitcnt vmcnt(0)
	v_mul_f32_e32 v7, v5, v1
